# speedup vs baseline: 1.0007x; 1.0007x over previous
.LBB3_11:
	s_lshl_b32 s58, s42, 7
	s_add_i32 s59, s41, 0x400
	s_lshr_b32 s59, s59, 6
	s_bfe_u32 s60, s20, 0x1000c
	s_add_i32 s59, s59, s60
	s_lshl_b32 s59, s59, 19
	s_add_u32 s58, s58, s59
	s_add_u32 s58, s56, s58
	s_addc_u32 s59, s57, 0
	s_add_u32 s60, s58, 0x4000
	s_addc_u32 s61, s59, 0
	s_add_u32 s62, s58, 0x100000
	s_addc_u32 s63, s59, 0
	s_add_u32 s64, s62, 0x4000
	s_addc_u32 s65, s63, 0
	s_lshr_b32 s66, s41, 7
	s_bfe_u32 s67, s20, 0x1000c
	s_add_i32 s66, s66, s67
	s_lshl_b32 s66, s66, 14
	s_lshl_b32 s67, s42, 2
	s_add_u32 s66, s66, s67
	s_add_u32 s66, s14, s66
	s_addc_u32 s67, s15, 0
	v_add_u32_e32 v172, s43, v207
	v_pk_fma_f32 v[244:245], v[244:245], -0.5, -0.5 op_sel_hi:[1,0,0]
	v_pk_fma_f32 v[246:247], v[246:247], -0.5, -0.5 op_sel_hi:[1,0,0]
	v_pk_fma_f32 v[248:249], v[248:249], -0.5, -0.5 op_sel_hi:[1,0,0]
	v_pk_fma_f32 v[250:251], v[250:251], -0.5, -0.5 op_sel_hi:[1,0,0]
	v_pk_fma_f32 v[252:253], v[252:253], -0.5, -0.5 op_sel_hi:[1,0,0]
	v_pk_fma_f32 v[254:255], v[254:255], -0.5, -0.5 op_sel_hi:[1,0,0]
	v_pk_fma_f32 v[232:233], v[232:233], -0.5, -0.5 op_sel_hi:[1,0,0]
	v_pk_fma_f32 v[234:235], v[234:235], -0.5, -0.5 op_sel_hi:[1,0,0]
	v_pk_mul_f32 v[134:135], v[244:245], v[246:247]
	v_pk_mul_f32 v[146:147], v[248:249], v[250:251]
	v_pk_mul_f32 v[180:181], v[252:253], v[254:255]
	v_pk_mul_f32 v[236:237], v[232:233], v[234:235]
	v_mul_f32_e32 v188, v134, v135
	v_mul_f32_e32 v190, v146, v147
	v_mul_f32_e32 v189, v180, v181
	v_mul_f32_e32 v191, v236, v237
	v_pk_mul_f32 v[192:193], v[188:189], v[190:191]
	v_mul_f32_e32 v162, v192, v193
	v_rcp_f32_e32 v173, v162
	v_pk_add_f32 v[164:165], v[114:115], v[116:117]
	v_pk_add_f32 v[164:165], v[164:165], v[78:79]
	v_pk_add_f32 v[164:165], v[164:165], v[80:81]
	v_pk_add_f32 v[164:165], v[164:165], v[106:107]
	v_pk_add_f32 v[164:165], v[164:165], v[108:109]
	v_pk_add_f32 v[164:165], v[164:165], v[70:71]
	v_pk_add_f32 v[164:165], v[164:165], v[72:73]
	v_pk_mul_f32 v[230:231], v[172:173], v[192:193] op_sel:[1,1] op_sel_hi:[1,0]
	v_pk_mul_f32 v[192:193], v[230:231], v[190:191]
	v_pk_mul_f32 v[190:191], v[230:231], v[188:189]
	v_pk_mul_f32 v[136:137], v[192:193], v[134:135] op_sel:[0,1] op_sel_hi:[0,0]
	v_pk_mul_f32 v[148:149], v[190:191], v[146:147] op_sel:[0,1] op_sel_hi:[0,0]
	v_pk_mul_f32 v[182:183], v[192:193], v[180:181] op_sel:[1,1] op_sel_hi:[1,0]
	v_pk_mul_f32 v[238:239], v[190:191], v[236:237] op_sel:[1,1] op_sel_hi:[1,0]
	v_pk_fma_f32 v[138:139], v[136:137], v[246:247], 1.0 op_sel_hi:[1,1,0]
	v_pk_fma_f32 v[140:141], v[136:137], v[244:245], 1.0 op_sel_hi:[1,1,0]
	v_pk_fma_f32 v[150:151], v[148:149], v[250:251], 1.0 op_sel_hi:[1,1,0]
	v_pk_fma_f32 v[152:153], v[148:149], v[248:249], 1.0 op_sel_hi:[1,1,0]
	v_pk_fma_f32 v[184:185], v[182:183], v[254:255], 1.0 op_sel_hi:[1,1,0]
	v_pk_fma_f32 v[186:187], v[182:183], v[252:253], 1.0 op_sel_hi:[1,1,0]
	v_pk_fma_f32 v[240:241], v[238:239], v[234:235], 1.0 op_sel_hi:[1,1,0]
	v_pk_fma_f32 v[242:243], v[238:239], v[232:233], 1.0 op_sel_hi:[1,1,0]
	v_cvt_pk_bf16_f32 v154, v138, v139
	v_cvt_pk_bf16_f32 v155, v140, v141
	v_cvt_pk_bf16_f32 v156, v150, v151
	v_cvt_pk_bf16_f32 v157, v152, v153
	v_cvt_pk_bf16_f32 v158, v184, v185
	v_cvt_pk_bf16_f32 v159, v186, v187
	v_cvt_pk_bf16_f32 v160, v240, v241
	v_cvt_pk_bf16_f32 v161, v242, v243
	ds_read_b128 v[114:117], v172
	ds_read_b128 v[78:81], v172 offset:64
	ds_read_b128 v[106:109], v172 offset:128
	ds_read_b128 v[70:73], v172 offset:192
	v_permlane16_swap_b32_e32 v154, v156
	v_permlane16_swap_b32_e32 v155, v157
	global_store_dwordx4 v228, v[154:157], s[58:59] nt
	v_permlane16_swap_b32_e32 v158, v160
	v_permlane16_swap_b32_e32 v159, v161
	global_store_dwordx4 v228, v[158:161], s[58:59] offset:128 nt
	v_exp_f32_e32 v130, v90
	v_exp_f32_e32 v131, v91
	v_exp_f32_e32 v132, v92
	v_exp_f32_e32 v133, v93
	v_exp_f32_e32 v142, v42
	v_exp_f32_e32 v143, v43
	v_exp_f32_e32 v144, v44
	v_exp_f32_e32 v145, v45
	v_exp_f32_e32 v176, v126
	v_exp_f32_e32 v177, v127
	v_exp_f32_e32 v178, v128
	v_exp_f32_e32 v179, v129
	v_exp_f32_e32 v232, v58
	v_exp_f32_e32 v233, v59
	v_exp_f32_e32 v234, v60
	v_exp_f32_e32 v235, v61
	s_bitcmp1_b32 s20, 12
	s_cbranch_scc1 .Lg1_noX
	s_barrier
.Lg1_noX:
	v_pk_fma_f32 v[130:131], v[130:131], -0.5, -0.5 op_sel_hi:[1,0,0]
	v_pk_fma_f32 v[132:133], v[132:133], -0.5, -0.5 op_sel_hi:[1,0,0]
	v_pk_fma_f32 v[142:143], v[142:143], -0.5, -0.5 op_sel_hi:[1,0,0]
	v_pk_fma_f32 v[144:145], v[144:145], -0.5, -0.5 op_sel_hi:[1,0,0]
	v_pk_fma_f32 v[176:177], v[176:177], -0.5, -0.5 op_sel_hi:[1,0,0]
	v_pk_fma_f32 v[178:179], v[178:179], -0.5, -0.5 op_sel_hi:[1,0,0]
	v_pk_fma_f32 v[232:233], v[232:233], -0.5, -0.5 op_sel_hi:[1,0,0]
	v_pk_fma_f32 v[234:235], v[234:235], -0.5, -0.5 op_sel_hi:[1,0,0]
	v_pk_mul_f32 v[134:135], v[130:131], v[132:133]
	v_pk_mul_f32 v[146:147], v[142:143], v[144:145]
	v_pk_mul_f32 v[180:181], v[176:177], v[178:179]
	v_pk_mul_f32 v[236:237], v[232:233], v[234:235]
	v_mul_f32_e32 v188, v134, v135
	v_mul_f32_e32 v190, v146, v147
	v_mul_f32_e32 v189, v180, v181
	v_mul_f32_e32 v191, v236, v237
	v_pk_mul_f32 v[192:193], v[188:189], v[190:191]
	v_mul_f32_e32 v174, v192, v193
	v_rcp_f32_e32 v173, v174
	v_pk_add_f32 v[164:165], v[164:165], v[90:91]
	v_pk_add_f32 v[164:165], v[164:165], v[92:93]
	v_pk_add_f32 v[164:165], v[164:165], v[42:43]
	v_pk_add_f32 v[164:165], v[164:165], v[44:45]
	v_pk_add_f32 v[164:165], v[164:165], v[126:127]
	v_pk_add_f32 v[164:165], v[164:165], v[128:129]
	v_pk_add_f32 v[164:165], v[164:165], v[58:59]
	v_pk_add_f32 v[164:165], v[164:165], v[60:61]
	v_pk_mul_f32 v[230:231], v[172:173], v[192:193] op_sel:[1,1] op_sel_hi:[1,0]
	v_pk_mul_f32 v[192:193], v[230:231], v[190:191]
	v_pk_mul_f32 v[190:191], v[230:231], v[188:189]
	v_pk_mul_f32 v[136:137], v[192:193], v[134:135] op_sel:[0,1] op_sel_hi:[0,0]
	v_pk_mul_f32 v[148:149], v[190:191], v[146:147] op_sel:[0,1] op_sel_hi:[0,0]
	v_pk_mul_f32 v[182:183], v[192:193], v[180:181] op_sel:[1,1] op_sel_hi:[1,0]
	v_pk_mul_f32 v[238:239], v[190:191], v[236:237] op_sel:[1,1] op_sel_hi:[1,0]
	v_pk_fma_f32 v[138:139], v[136:137], v[132:133], 1.0 op_sel_hi:[1,1,0]
	v_pk_fma_f32 v[140:141], v[136:137], v[130:131], 1.0 op_sel_hi:[1,1,0]
	v_pk_fma_f32 v[150:151], v[148:149], v[144:145], 1.0 op_sel_hi:[1,1,0]
	v_pk_fma_f32 v[152:153], v[148:149], v[142:143], 1.0 op_sel_hi:[1,1,0]
	v_pk_fma_f32 v[184:185], v[182:183], v[178:179], 1.0 op_sel_hi:[1,1,0]
	v_pk_fma_f32 v[186:187], v[182:183], v[176:177], 1.0 op_sel_hi:[1,1,0]
	v_pk_fma_f32 v[240:241], v[238:239], v[234:235], 1.0 op_sel_hi:[1,1,0]
	v_pk_fma_f32 v[242:243], v[238:239], v[232:233], 1.0 op_sel_hi:[1,1,0]
	v_cvt_pk_bf16_f32 v154, v138, v139
	v_cvt_pk_bf16_f32 v155, v140, v141
	v_cvt_pk_bf16_f32 v156, v150, v151
	v_cvt_pk_bf16_f32 v157, v152, v153
	v_cvt_pk_bf16_f32 v158, v184, v185
	v_cvt_pk_bf16_f32 v159, v186, v187
	v_cvt_pk_bf16_f32 v160, v240, v241
	v_cvt_pk_bf16_f32 v161, v242, v243
	ds_read_b128 v[90:93], v172 offset:512
	ds_read_b128 v[42:45], v172 offset:576
	ds_read_b128 v[126:129], v172 offset:640
	ds_read_b128 v[58:61], v172 offset:704
	v_permlane16_swap_b32_e32 v154, v156
	v_permlane16_swap_b32_e32 v155, v157
	global_store_dwordx4 v228, v[154:157], s[62:63] nt
	v_permlane16_swap_b32_e32 v158, v160
	v_permlane16_swap_b32_e32 v159, v161
	global_store_dwordx4 v228, v[158:161], s[62:63] offset:128 nt
	v_log_f32_e32 v166, v162
	v_log_f32_e32 v170, v174
	v_add_f32_e32 v168, v164, v165
	v_mul_f32_e32 v168, 0xbeb17218, v168
	v_add_f32_e32 v166, v166, v170
	v_fmac_f32_e32 v168, 0x3f317218, v166
	v_mov_b32_e32 v169, v168
	s_nop 1
	v_permlane16_swap_b32_e32 v168, v169
	v_add_f32_e32 v168, v168, v169
	v_mov_b32_e32 v169, v168
	s_nop 1
	v_permlane32_swap_b32_e32 v168, v169
	v_add_f32_e32 v168, v168, v169
	s_mov_b64 exec, s[0:1]
	global_store_dword v229, v168, s[66:67]
	s_mov_b64 exec, -1
	v_exp_f32_e32 v130, v110
	v_exp_f32_e32 v131, v111
	v_exp_f32_e32 v132, v112
	v_exp_f32_e32 v133, v113
	v_exp_f32_e32 v142, v74
	v_exp_f32_e32 v143, v75
	v_exp_f32_e32 v144, v76
	v_exp_f32_e32 v145, v77
	v_exp_f32_e32 v176, v102
	v_exp_f32_e32 v177, v103
	v_exp_f32_e32 v178, v104
	v_exp_f32_e32 v179, v105
	v_exp_f32_e32 v232, v66
	v_exp_f32_e32 v233, v67
	v_exp_f32_e32 v234, v68
	v_exp_f32_e32 v235, v69
	v_pk_fma_f32 v[130:131], v[130:131], -0.5, -0.5 op_sel_hi:[1,0,0]
	v_pk_fma_f32 v[132:133], v[132:133], -0.5, -0.5 op_sel_hi:[1,0,0]
	v_pk_fma_f32 v[142:143], v[142:143], -0.5, -0.5 op_sel_hi:[1,0,0]
	v_pk_fma_f32 v[144:145], v[144:145], -0.5, -0.5 op_sel_hi:[1,0,0]
	v_pk_fma_f32 v[176:177], v[176:177], -0.5, -0.5 op_sel_hi:[1,0,0]
	v_pk_fma_f32 v[178:179], v[178:179], -0.5, -0.5 op_sel_hi:[1,0,0]
	v_pk_fma_f32 v[232:233], v[232:233], -0.5, -0.5 op_sel_hi:[1,0,0]
	v_pk_fma_f32 v[234:235], v[234:235], -0.5, -0.5 op_sel_hi:[1,0,0]
	v_pk_mul_f32 v[134:135], v[130:131], v[132:133]
	v_pk_mul_f32 v[146:147], v[142:143], v[144:145]
	v_pk_mul_f32 v[180:181], v[176:177], v[178:179]
	v_pk_mul_f32 v[236:237], v[232:233], v[234:235]
	v_mul_f32_e32 v188, v134, v135
	v_mul_f32_e32 v190, v146, v147
	v_mul_f32_e32 v189, v180, v181
	v_mul_f32_e32 v191, v236, v237
	v_pk_mul_f32 v[192:193], v[188:189], v[190:191]
	v_mul_f32_e32 v162, v192, v193
	v_rcp_f32_e32 v173, v162
	v_pk_add_f32 v[164:165], v[110:111], v[112:113]
	v_pk_add_f32 v[164:165], v[164:165], v[74:75]
	v_pk_add_f32 v[164:165], v[164:165], v[76:77]
	v_pk_add_f32 v[164:165], v[164:165], v[102:103]
	v_pk_add_f32 v[164:165], v[164:165], v[104:105]
	v_pk_add_f32 v[164:165], v[164:165], v[66:67]
	v_pk_add_f32 v[164:165], v[164:165], v[68:69]
	v_pk_mul_f32 v[230:231], v[172:173], v[192:193] op_sel:[1,1] op_sel_hi:[1,0]
	v_pk_mul_f32 v[192:193], v[230:231], v[190:191]
	v_pk_mul_f32 v[190:191], v[230:231], v[188:189]
	v_pk_mul_f32 v[136:137], v[192:193], v[134:135] op_sel:[0,1] op_sel_hi:[0,0]
	v_pk_mul_f32 v[148:149], v[190:191], v[146:147] op_sel:[0,1] op_sel_hi:[0,0]
	v_pk_mul_f32 v[182:183], v[192:193], v[180:181] op_sel:[1,1] op_sel_hi:[1,0]
	v_pk_mul_f32 v[238:239], v[190:191], v[236:237] op_sel:[1,1] op_sel_hi:[1,0]
	v_pk_fma_f32 v[138:139], v[136:137], v[132:133], 1.0 op_sel_hi:[1,1,0]
	v_pk_fma_f32 v[140:141], v[136:137], v[130:131], 1.0 op_sel_hi:[1,1,0]
	v_pk_fma_f32 v[150:151], v[148:149], v[144:145], 1.0 op_sel_hi:[1,1,0]
	v_pk_fma_f32 v[152:153], v[148:149], v[142:143], 1.0 op_sel_hi:[1,1,0]
	v_pk_fma_f32 v[184:185], v[182:183], v[178:179], 1.0 op_sel_hi:[1,1,0]
	v_pk_fma_f32 v[186:187], v[182:183], v[176:177], 1.0 op_sel_hi:[1,1,0]
	v_pk_fma_f32 v[240:241], v[238:239], v[234:235], 1.0 op_sel_hi:[1,1,0]
	v_pk_fma_f32 v[242:243], v[238:239], v[232:233], 1.0 op_sel_hi:[1,1,0]
	v_cvt_pk_bf16_f32 v154, v138, v139
	v_cvt_pk_bf16_f32 v155, v140, v141
	v_cvt_pk_bf16_f32 v156, v150, v151
	v_cvt_pk_bf16_f32 v157, v152, v153
	v_cvt_pk_bf16_f32 v158, v184, v185
	v_cvt_pk_bf16_f32 v159, v186, v187
	v_cvt_pk_bf16_f32 v160, v240, v241
	v_cvt_pk_bf16_f32 v161, v242, v243
	ds_read_b128 v[110:113], v172
	ds_read_b128 v[74:77], v172 offset:64
	ds_read_b128 v[102:105], v172 offset:128
	ds_read_b128 v[66:69], v172 offset:192
	v_permlane16_swap_b32_e32 v154, v156
	v_permlane16_swap_b32_e32 v155, v157
	global_store_dwordx4 v228, v[154:157], s[58:59] offset:2048 nt
	v_permlane16_swap_b32_e32 v158, v160
	v_permlane16_swap_b32_e32 v159, v161
	global_store_dwordx4 v228, v[158:161], s[58:59] offset:2176 nt
	v_exp_f32_e32 v130, v86
	v_exp_f32_e32 v131, v87
	v_exp_f32_e32 v132, v88
	v_exp_f32_e32 v133, v89
	v_exp_f32_e32 v142, v38
	v_exp_f32_e32 v143, v39
	v_exp_f32_e32 v144, v40
	v_exp_f32_e32 v145, v41
	v_exp_f32_e32 v176, v122
	v_exp_f32_e32 v177, v123
	v_exp_f32_e32 v178, v124
	v_exp_f32_e32 v179, v125
	v_exp_f32_e32 v232, v50
	v_exp_f32_e32 v233, v51
	v_exp_f32_e32 v234, v52
	v_exp_f32_e32 v235, v53
	v_pk_fma_f32 v[130:131], v[130:131], -0.5, -0.5 op_sel_hi:[1,0,0]
	v_pk_fma_f32 v[132:133], v[132:133], -0.5, -0.5 op_sel_hi:[1,0,0]
	v_pk_fma_f32 v[142:143], v[142:143], -0.5, -0.5 op_sel_hi:[1,0,0]
	v_pk_fma_f32 v[144:145], v[144:145], -0.5, -0.5 op_sel_hi:[1,0,0]
	v_pk_fma_f32 v[176:177], v[176:177], -0.5, -0.5 op_sel_hi:[1,0,0]
	v_pk_fma_f32 v[178:179], v[178:179], -0.5, -0.5 op_sel_hi:[1,0,0]
	v_pk_fma_f32 v[232:233], v[232:233], -0.5, -0.5 op_sel_hi:[1,0,0]
	v_pk_fma_f32 v[234:235], v[234:235], -0.5, -0.5 op_sel_hi:[1,0,0]
	v_pk_mul_f32 v[134:135], v[130:131], v[132:133]
	v_pk_mul_f32 v[146:147], v[142:143], v[144:145]
	v_pk_mul_f32 v[180:181], v[176:177], v[178:179]
	v_pk_mul_f32 v[236:237], v[232:233], v[234:235]
	v_mul_f32_e32 v188, v134, v135
	v_mul_f32_e32 v190, v146, v147
	v_mul_f32_e32 v189, v180, v181
	v_mul_f32_e32 v191, v236, v237
	v_pk_mul_f32 v[192:193], v[188:189], v[190:191]
	v_mul_f32_e32 v174, v192, v193
	v_rcp_f32_e32 v173, v174
	v_pk_add_f32 v[164:165], v[164:165], v[86:87]
	v_pk_add_f32 v[164:165], v[164:165], v[88:89]
	v_pk_add_f32 v[164:165], v[164:165], v[38:39]
	v_pk_add_f32 v[164:165], v[164:165], v[40:41]
	v_pk_add_f32 v[164:165], v[164:165], v[122:123]
	v_pk_add_f32 v[164:165], v[164:165], v[124:125]
	v_pk_add_f32 v[164:165], v[164:165], v[50:51]
	v_pk_add_f32 v[164:165], v[164:165], v[52:53]
	v_pk_mul_f32 v[230:231], v[172:173], v[192:193] op_sel:[1,1] op_sel_hi:[1,0]
	v_pk_mul_f32 v[192:193], v[230:231], v[190:191]
	v_pk_mul_f32 v[190:191], v[230:231], v[188:189]
	v_pk_mul_f32 v[136:137], v[192:193], v[134:135] op_sel:[0,1] op_sel_hi:[0,0]
	v_pk_mul_f32 v[148:149], v[190:191], v[146:147] op_sel:[0,1] op_sel_hi:[0,0]
	v_pk_mul_f32 v[182:183], v[192:193], v[180:181] op_sel:[1,1] op_sel_hi:[1,0]
	v_pk_mul_f32 v[238:239], v[190:191], v[236:237] op_sel:[1,1] op_sel_hi:[1,0]
	v_pk_fma_f32 v[138:139], v[136:137], v[132:133], 1.0 op_sel_hi:[1,1,0]
	v_pk_fma_f32 v[140:141], v[136:137], v[130:131], 1.0 op_sel_hi:[1,1,0]
	v_pk_fma_f32 v[150:151], v[148:149], v[144:145], 1.0 op_sel_hi:[1,1,0]
	v_pk_fma_f32 v[152:153], v[148:149], v[142:143], 1.0 op_sel_hi:[1,1,0]
	v_pk_fma_f32 v[184:185], v[182:183], v[178:179], 1.0 op_sel_hi:[1,1,0]
	v_pk_fma_f32 v[186:187], v[182:183], v[176:177], 1.0 op_sel_hi:[1,1,0]
	v_pk_fma_f32 v[240:241], v[238:239], v[234:235], 1.0 op_sel_hi:[1,1,0]
	v_pk_fma_f32 v[242:243], v[238:239], v[232:233], 1.0 op_sel_hi:[1,1,0]
	v_cvt_pk_bf16_f32 v154, v138, v139
	v_cvt_pk_bf16_f32 v155, v140, v141
	v_cvt_pk_bf16_f32 v156, v150, v151
	v_cvt_pk_bf16_f32 v157, v152, v153
	v_cvt_pk_bf16_f32 v158, v184, v185
	v_cvt_pk_bf16_f32 v159, v186, v187
	v_cvt_pk_bf16_f32 v160, v240, v241
	v_cvt_pk_bf16_f32 v161, v242, v243
	ds_read_b128 v[86:89], v172 offset:512
	ds_read_b128 v[38:41], v172 offset:576
	ds_read_b128 v[122:125], v172 offset:640
	ds_read_b128 v[50:53], v172 offset:704
	v_permlane16_swap_b32_e32 v154, v156
	v_permlane16_swap_b32_e32 v155, v157
	global_store_dwordx4 v228, v[154:157], s[62:63] offset:2048 nt
	v_permlane16_swap_b32_e32 v158, v160
	v_permlane16_swap_b32_e32 v159, v161
	global_store_dwordx4 v228, v[158:161], s[62:63] offset:2176 nt
	v_log_f32_e32 v166, v162
	v_log_f32_e32 v170, v174
	v_add_f32_e32 v168, v164, v165
	v_mul_f32_e32 v168, 0xbeb17218, v168
	v_add_f32_e32 v166, v166, v170
	v_fmac_f32_e32 v168, 0x3f317218, v166
	v_mov_b32_e32 v169, v168
	s_nop 1
	v_permlane16_swap_b32_e32 v168, v169
	v_add_f32_e32 v168, v168, v169
	v_mov_b32_e32 v169, v168
	s_nop 1
	v_permlane32_swap_b32_e32 v168, v169
	v_add_f32_e32 v168, v168, v169
	s_mov_b64 exec, s[0:1]
	global_store_dword v229, v168, s[66:67] offset:64
	s_mov_b64 exec, -1
	v_exp_f32_e32 v130, v98
	v_exp_f32_e32 v131, v99
	v_exp_f32_e32 v132, v100
	v_exp_f32_e32 v133, v101
	v_exp_f32_e32 v142, v62
	v_exp_f32_e32 v143, v63
	v_exp_f32_e32 v144, v64
	v_exp_f32_e32 v145, v65
	v_exp_f32_e32 v176, v94
	v_exp_f32_e32 v177, v95
	v_exp_f32_e32 v178, v96
	v_exp_f32_e32 v179, v97
	v_exp_f32_e32 v232, v54
	v_exp_f32_e32 v233, v55
	v_exp_f32_e32 v234, v56
	v_exp_f32_e32 v235, v57
	v_pk_fma_f32 v[130:131], v[130:131], -0.5, -0.5 op_sel_hi:[1,0,0]
	v_pk_fma_f32 v[132:133], v[132:133], -0.5, -0.5 op_sel_hi:[1,0,0]
	v_pk_fma_f32 v[142:143], v[142:143], -0.5, -0.5 op_sel_hi:[1,0,0]
	v_pk_fma_f32 v[144:145], v[144:145], -0.5, -0.5 op_sel_hi:[1,0,0]
	v_pk_fma_f32 v[176:177], v[176:177], -0.5, -0.5 op_sel_hi:[1,0,0]
	v_pk_fma_f32 v[178:179], v[178:179], -0.5, -0.5 op_sel_hi:[1,0,0]
	v_pk_fma_f32 v[232:233], v[232:233], -0.5, -0.5 op_sel_hi:[1,0,0]
	v_pk_fma_f32 v[234:235], v[234:235], -0.5, -0.5 op_sel_hi:[1,0,0]
	v_pk_mul_f32 v[134:135], v[130:131], v[132:133]
	v_pk_mul_f32 v[146:147], v[142:143], v[144:145]
	v_pk_mul_f32 v[180:181], v[176:177], v[178:179]
	v_pk_mul_f32 v[236:237], v[232:233], v[234:235]
	v_mul_f32_e32 v188, v134, v135
	v_mul_f32_e32 v190, v146, v147
	v_mul_f32_e32 v189, v180, v181
	v_mul_f32_e32 v191, v236, v237
	v_pk_mul_f32 v[192:193], v[188:189], v[190:191]
	v_mul_f32_e32 v162, v192, v193
	v_rcp_f32_e32 v173, v162
	v_pk_add_f32 v[164:165], v[98:99], v[100:101]
	v_pk_add_f32 v[164:165], v[164:165], v[62:63]
	v_pk_add_f32 v[164:165], v[164:165], v[64:65]
	v_pk_add_f32 v[164:165], v[164:165], v[94:95]
	v_pk_add_f32 v[164:165], v[164:165], v[96:97]
	v_pk_add_f32 v[164:165], v[164:165], v[54:55]
	v_pk_add_f32 v[164:165], v[164:165], v[56:57]
	v_pk_mul_f32 v[230:231], v[172:173], v[192:193] op_sel:[1,1] op_sel_hi:[1,0]
	v_pk_mul_f32 v[192:193], v[230:231], v[190:191]
	v_pk_mul_f32 v[190:191], v[230:231], v[188:189]
	v_pk_mul_f32 v[136:137], v[192:193], v[134:135] op_sel:[0,1] op_sel_hi:[0,0]
	v_pk_mul_f32 v[148:149], v[190:191], v[146:147] op_sel:[0,1] op_sel_hi:[0,0]
	v_pk_mul_f32 v[182:183], v[192:193], v[180:181] op_sel:[1,1] op_sel_hi:[1,0]
	v_pk_mul_f32 v[238:239], v[190:191], v[236:237] op_sel:[1,1] op_sel_hi:[1,0]
	v_pk_fma_f32 v[138:139], v[136:137], v[132:133], 1.0 op_sel_hi:[1,1,0]
	v_pk_fma_f32 v[140:141], v[136:137], v[130:131], 1.0 op_sel_hi:[1,1,0]
	v_pk_fma_f32 v[150:151], v[148:149], v[144:145], 1.0 op_sel_hi:[1,1,0]
	v_pk_fma_f32 v[152:153], v[148:149], v[142:143], 1.0 op_sel_hi:[1,1,0]
	v_pk_fma_f32 v[184:185], v[182:183], v[178:179], 1.0 op_sel_hi:[1,1,0]
	v_pk_fma_f32 v[186:187], v[182:183], v[176:177], 1.0 op_sel_hi:[1,1,0]
	v_pk_fma_f32 v[240:241], v[238:239], v[234:235], 1.0 op_sel_hi:[1,1,0]
	v_pk_fma_f32 v[242:243], v[238:239], v[232:233], 1.0 op_sel_hi:[1,1,0]
	v_cvt_pk_bf16_f32 v154, v138, v139
	v_cvt_pk_bf16_f32 v155, v140, v141
	v_cvt_pk_bf16_f32 v156, v150, v151
	v_cvt_pk_bf16_f32 v157, v152, v153
	v_cvt_pk_bf16_f32 v158, v184, v185
	v_cvt_pk_bf16_f32 v159, v186, v187
	v_cvt_pk_bf16_f32 v160, v240, v241
	v_cvt_pk_bf16_f32 v161, v242, v243
	ds_read_b128 v[98:101], v172
	ds_read_b128 v[62:65], v172 offset:64
	ds_read_b128 v[94:97], v172 offset:128
	ds_read_b128 v[54:57], v172 offset:192
	v_permlane16_swap_b32_e32 v154, v156
	v_permlane16_swap_b32_e32 v155, v157
	global_store_dwordx4 v228, v[154:157], s[60:61] nt
	v_permlane16_swap_b32_e32 v158, v160
	v_permlane16_swap_b32_e32 v159, v161
	global_store_dwordx4 v228, v[158:161], s[60:61] offset:128 nt
	v_exp_f32_e32 v130, v82
	v_exp_f32_e32 v131, v83
	v_exp_f32_e32 v132, v84
	v_exp_f32_e32 v133, v85
	v_exp_f32_e32 v142, v34
	v_exp_f32_e32 v143, v35
	v_exp_f32_e32 v144, v36
	v_exp_f32_e32 v145, v37
	v_exp_f32_e32 v176, v118
	v_exp_f32_e32 v177, v119
	v_exp_f32_e32 v178, v120
	v_exp_f32_e32 v179, v121
	v_exp_f32_e32 v232, v46
	v_exp_f32_e32 v233, v47
	v_exp_f32_e32 v234, v48
	v_exp_f32_e32 v235, v49
	v_pk_fma_f32 v[130:131], v[130:131], -0.5, -0.5 op_sel_hi:[1,0,0]
	v_pk_fma_f32 v[132:133], v[132:133], -0.5, -0.5 op_sel_hi:[1,0,0]
	v_pk_fma_f32 v[142:143], v[142:143], -0.5, -0.5 op_sel_hi:[1,0,0]
	v_pk_fma_f32 v[144:145], v[144:145], -0.5, -0.5 op_sel_hi:[1,0,0]
	v_pk_fma_f32 v[176:177], v[176:177], -0.5, -0.5 op_sel_hi:[1,0,0]
	v_pk_fma_f32 v[178:179], v[178:179], -0.5, -0.5 op_sel_hi:[1,0,0]
	v_pk_fma_f32 v[232:233], v[232:233], -0.5, -0.5 op_sel_hi:[1,0,0]
	v_pk_fma_f32 v[234:235], v[234:235], -0.5, -0.5 op_sel_hi:[1,0,0]
	v_pk_mul_f32 v[134:135], v[130:131], v[132:133]
	v_pk_mul_f32 v[146:147], v[142:143], v[144:145]
	v_pk_mul_f32 v[180:181], v[176:177], v[178:179]
	v_pk_mul_f32 v[236:237], v[232:233], v[234:235]
	v_mul_f32_e32 v188, v134, v135
	v_mul_f32_e32 v190, v146, v147
	v_mul_f32_e32 v189, v180, v181
	v_mul_f32_e32 v191, v236, v237
	v_pk_mul_f32 v[192:193], v[188:189], v[190:191]
	v_mul_f32_e32 v174, v192, v193
	v_rcp_f32_e32 v173, v174
	v_pk_add_f32 v[164:165], v[164:165], v[82:83]
	v_pk_add_f32 v[164:165], v[164:165], v[84:85]
	v_pk_add_f32 v[164:165], v[164:165], v[34:35]
	v_pk_add_f32 v[164:165], v[164:165], v[36:37]
	v_pk_add_f32 v[164:165], v[164:165], v[118:119]
	v_pk_add_f32 v[164:165], v[164:165], v[120:121]
	v_pk_add_f32 v[164:165], v[164:165], v[46:47]
	v_pk_add_f32 v[164:165], v[164:165], v[48:49]
	v_pk_mul_f32 v[230:231], v[172:173], v[192:193] op_sel:[1,1] op_sel_hi:[1,0]
	v_pk_mul_f32 v[192:193], v[230:231], v[190:191]
	v_pk_mul_f32 v[190:191], v[230:231], v[188:189]
	v_pk_mul_f32 v[136:137], v[192:193], v[134:135] op_sel:[0,1] op_sel_hi:[0,0]
	v_pk_mul_f32 v[148:149], v[190:191], v[146:147] op_sel:[0,1] op_sel_hi:[0,0]
	v_pk_mul_f32 v[182:183], v[192:193], v[180:181] op_sel:[1,1] op_sel_hi:[1,0]
	v_pk_mul_f32 v[238:239], v[190:191], v[236:237] op_sel:[1,1] op_sel_hi:[1,0]
	v_pk_fma_f32 v[138:139], v[136:137], v[132:133], 1.0 op_sel_hi:[1,1,0]
	v_pk_fma_f32 v[140:141], v[136:137], v[130:131], 1.0 op_sel_hi:[1,1,0]
	v_pk_fma_f32 v[150:151], v[148:149], v[144:145], 1.0 op_sel_hi:[1,1,0]
	v_pk_fma_f32 v[152:153], v[148:149], v[142:143], 1.0 op_sel_hi:[1,1,0]
	v_pk_fma_f32 v[184:185], v[182:183], v[178:179], 1.0 op_sel_hi:[1,1,0]
	v_pk_fma_f32 v[186:187], v[182:183], v[176:177], 1.0 op_sel_hi:[1,1,0]
	v_pk_fma_f32 v[240:241], v[238:239], v[234:235], 1.0 op_sel_hi:[1,1,0]
	v_pk_fma_f32 v[242:243], v[238:239], v[232:233], 1.0 op_sel_hi:[1,1,0]
	v_cvt_pk_bf16_f32 v154, v138, v139
	v_cvt_pk_bf16_f32 v155, v140, v141
	v_cvt_pk_bf16_f32 v156, v150, v151
	v_cvt_pk_bf16_f32 v157, v152, v153
	v_cvt_pk_bf16_f32 v158, v184, v185
	v_cvt_pk_bf16_f32 v159, v186, v187
	v_cvt_pk_bf16_f32 v160, v240, v241
	v_cvt_pk_bf16_f32 v161, v242, v243
	ds_read_b128 v[82:85], v172 offset:512
	ds_read_b128 v[34:37], v172 offset:576
	ds_read_b128 v[118:121], v172 offset:640
	ds_read_b128 v[46:49], v172 offset:704
	v_permlane16_swap_b32_e32 v154, v156
	v_permlane16_swap_b32_e32 v155, v157
	global_store_dwordx4 v228, v[154:157], s[64:65] nt
	v_permlane16_swap_b32_e32 v158, v160
	v_permlane16_swap_b32_e32 v159, v161
	global_store_dwordx4 v228, v[158:161], s[64:65] offset:128 nt
	v_log_f32_e32 v166, v162
	v_log_f32_e32 v170, v174
	v_add_f32_e32 v168, v164, v165
	v_mul_f32_e32 v168, 0xbeb17218, v168
	v_add_f32_e32 v166, v166, v170
	v_fmac_f32_e32 v168, 0x3f317218, v166
	v_mov_b32_e32 v169, v168
	s_nop 1
	v_permlane16_swap_b32_e32 v168, v169
	v_add_f32_e32 v168, v168, v169
	v_mov_b32_e32 v169, v168
	s_nop 1
	v_permlane32_swap_b32_e32 v168, v169
	v_add_f32_e32 v168, v168, v169
	s_mov_b64 exec, s[0:1]
	global_store_dword v229, v168, s[66:67] offset:512
	s_mov_b64 exec, -1
	v_exp_f32_e32 v130, v18
	v_exp_f32_e32 v131, v19
	v_exp_f32_e32 v132, v20
	v_exp_f32_e32 v133, v21
	v_exp_f32_e32 v142, v2
	v_exp_f32_e32 v143, v3
	v_exp_f32_e32 v144, v4
	v_exp_f32_e32 v145, v5
	v_exp_f32_e32 v176, v26
	v_exp_f32_e32 v177, v27
	v_exp_f32_e32 v178, v28
	v_exp_f32_e32 v179, v29
	v_exp_f32_e32 v232, v10
	v_exp_f32_e32 v233, v11
	v_exp_f32_e32 v234, v12
	v_exp_f32_e32 v235, v13
	v_pk_fma_f32 v[130:131], v[130:131], -0.5, -0.5 op_sel_hi:[1,0,0]
	v_pk_fma_f32 v[132:133], v[132:133], -0.5, -0.5 op_sel_hi:[1,0,0]
	v_pk_fma_f32 v[142:143], v[142:143], -0.5, -0.5 op_sel_hi:[1,0,0]
	v_pk_fma_f32 v[144:145], v[144:145], -0.5, -0.5 op_sel_hi:[1,0,0]
	v_pk_fma_f32 v[176:177], v[176:177], -0.5, -0.5 op_sel_hi:[1,0,0]
	v_pk_fma_f32 v[178:179], v[178:179], -0.5, -0.5 op_sel_hi:[1,0,0]
	v_pk_fma_f32 v[232:233], v[232:233], -0.5, -0.5 op_sel_hi:[1,0,0]
	v_pk_fma_f32 v[234:235], v[234:235], -0.5, -0.5 op_sel_hi:[1,0,0]
	v_pk_mul_f32 v[134:135], v[130:131], v[132:133]
	v_pk_mul_f32 v[146:147], v[142:143], v[144:145]
	v_pk_mul_f32 v[180:181], v[176:177], v[178:179]
	v_pk_mul_f32 v[236:237], v[232:233], v[234:235]
	v_mul_f32_e32 v188, v134, v135
	v_mul_f32_e32 v190, v146, v147
	v_mul_f32_e32 v189, v180, v181
	v_mul_f32_e32 v191, v236, v237
	v_pk_mul_f32 v[192:193], v[188:189], v[190:191]
	v_mul_f32_e32 v162, v192, v193
	v_rcp_f32_e32 v173, v162
	v_pk_add_f32 v[164:165], v[18:19], v[20:21]
	v_pk_add_f32 v[164:165], v[164:165], v[2:3]
	v_pk_add_f32 v[164:165], v[164:165], v[4:5]
	v_pk_add_f32 v[164:165], v[164:165], v[26:27]
	v_pk_add_f32 v[164:165], v[164:165], v[28:29]
	v_pk_add_f32 v[164:165], v[164:165], v[10:11]
	v_pk_add_f32 v[164:165], v[164:165], v[12:13]
	v_pk_mul_f32 v[230:231], v[172:173], v[192:193] op_sel:[1,1] op_sel_hi:[1,0]
	v_pk_mul_f32 v[192:193], v[230:231], v[190:191]
	v_pk_mul_f32 v[190:191], v[230:231], v[188:189]
	v_pk_mul_f32 v[136:137], v[192:193], v[134:135] op_sel:[0,1] op_sel_hi:[0,0]
	v_pk_mul_f32 v[148:149], v[190:191], v[146:147] op_sel:[0,1] op_sel_hi:[0,0]
	v_pk_mul_f32 v[182:183], v[192:193], v[180:181] op_sel:[1,1] op_sel_hi:[1,0]
	v_pk_mul_f32 v[238:239], v[190:191], v[236:237] op_sel:[1,1] op_sel_hi:[1,0]
	v_pk_fma_f32 v[138:139], v[136:137], v[132:133], 1.0 op_sel_hi:[1,1,0]
	v_pk_fma_f32 v[140:141], v[136:137], v[130:131], 1.0 op_sel_hi:[1,1,0]
	v_pk_fma_f32 v[150:151], v[148:149], v[144:145], 1.0 op_sel_hi:[1,1,0]
	v_pk_fma_f32 v[152:153], v[148:149], v[142:143], 1.0 op_sel_hi:[1,1,0]
	v_pk_fma_f32 v[184:185], v[182:183], v[178:179], 1.0 op_sel_hi:[1,1,0]
	v_pk_fma_f32 v[186:187], v[182:183], v[176:177], 1.0 op_sel_hi:[1,1,0]
	v_pk_fma_f32 v[240:241], v[238:239], v[234:235], 1.0 op_sel_hi:[1,1,0]
	v_pk_fma_f32 v[242:243], v[238:239], v[232:233], 1.0 op_sel_hi:[1,1,0]
	v_cvt_pk_bf16_f32 v154, v138, v139
	v_cvt_pk_bf16_f32 v155, v140, v141
	v_cvt_pk_bf16_f32 v156, v150, v151
	v_cvt_pk_bf16_f32 v157, v152, v153
	v_cvt_pk_bf16_f32 v158, v184, v185
	v_cvt_pk_bf16_f32 v159, v186, v187
	v_cvt_pk_bf16_f32 v160, v240, v241
	v_cvt_pk_bf16_f32 v161, v242, v243
	ds_read_b128 v[18:21], v172
	ds_read_b128 v[2:5], v172 offset:64
	ds_read_b128 v[26:29], v172 offset:128
	ds_read_b128 v[10:13], v172 offset:192
	v_permlane16_swap_b32_e32 v154, v156
	v_permlane16_swap_b32_e32 v155, v157
	global_store_dwordx4 v228, v[154:157], s[60:61] offset:2048 nt
	v_permlane16_swap_b32_e32 v158, v160
	v_permlane16_swap_b32_e32 v159, v161
	global_store_dwordx4 v228, v[158:161], s[60:61] offset:2176 nt
	v_exp_f32_e32 v130, v22
	v_exp_f32_e32 v131, v23
	v_exp_f32_e32 v132, v24
	v_exp_f32_e32 v133, v25
	v_exp_f32_e32 v142, v6
	v_exp_f32_e32 v143, v7
	v_exp_f32_e32 v144, v8
	v_exp_f32_e32 v145, v9
	v_exp_f32_e32 v176, v30
	v_exp_f32_e32 v177, v31
	v_exp_f32_e32 v178, v32
	v_exp_f32_e32 v179, v33
	v_exp_f32_e32 v232, v14
	v_exp_f32_e32 v233, v15
	v_exp_f32_e32 v234, v16
	v_exp_f32_e32 v235, v17
	v_pk_fma_f32 v[130:131], v[130:131], -0.5, -0.5 op_sel_hi:[1,0,0]
	v_pk_fma_f32 v[132:133], v[132:133], -0.5, -0.5 op_sel_hi:[1,0,0]
	v_pk_fma_f32 v[142:143], v[142:143], -0.5, -0.5 op_sel_hi:[1,0,0]
	v_pk_fma_f32 v[144:145], v[144:145], -0.5, -0.5 op_sel_hi:[1,0,0]
	v_pk_fma_f32 v[176:177], v[176:177], -0.5, -0.5 op_sel_hi:[1,0,0]
	v_pk_fma_f32 v[178:179], v[178:179], -0.5, -0.5 op_sel_hi:[1,0,0]
	v_pk_fma_f32 v[232:233], v[232:233], -0.5, -0.5 op_sel_hi:[1,0,0]
	v_pk_fma_f32 v[234:235], v[234:235], -0.5, -0.5 op_sel_hi:[1,0,0]
	v_pk_mul_f32 v[134:135], v[130:131], v[132:133]
	v_pk_mul_f32 v[146:147], v[142:143], v[144:145]
	v_pk_mul_f32 v[180:181], v[176:177], v[178:179]
	v_pk_mul_f32 v[236:237], v[232:233], v[234:235]
	v_mul_f32_e32 v188, v134, v135
	v_mul_f32_e32 v190, v146, v147
	v_mul_f32_e32 v189, v180, v181
	v_mul_f32_e32 v191, v236, v237
	v_pk_mul_f32 v[192:193], v[188:189], v[190:191]
	v_mul_f32_e32 v174, v192, v193
	v_rcp_f32_e32 v173, v174
	v_pk_add_f32 v[164:165], v[164:165], v[22:23]
	v_pk_add_f32 v[164:165], v[164:165], v[24:25]
	v_pk_add_f32 v[164:165], v[164:165], v[6:7]
	v_pk_add_f32 v[164:165], v[164:165], v[8:9]
	v_pk_add_f32 v[164:165], v[164:165], v[30:31]
	v_pk_add_f32 v[164:165], v[164:165], v[32:33]
	v_pk_add_f32 v[164:165], v[164:165], v[14:15]
	v_pk_add_f32 v[164:165], v[164:165], v[16:17]
	v_pk_mul_f32 v[230:231], v[172:173], v[192:193] op_sel:[1,1] op_sel_hi:[1,0]
	v_pk_mul_f32 v[192:193], v[230:231], v[190:191]
	v_pk_mul_f32 v[190:191], v[230:231], v[188:189]
	v_pk_mul_f32 v[136:137], v[192:193], v[134:135] op_sel:[0,1] op_sel_hi:[0,0]
	v_pk_mul_f32 v[148:149], v[190:191], v[146:147] op_sel:[0,1] op_sel_hi:[0,0]
	v_pk_mul_f32 v[182:183], v[192:193], v[180:181] op_sel:[1,1] op_sel_hi:[1,0]
	v_pk_mul_f32 v[238:239], v[190:191], v[236:237] op_sel:[1,1] op_sel_hi:[1,0]
	v_pk_fma_f32 v[138:139], v[136:137], v[132:133], 1.0 op_sel_hi:[1,1,0]
	v_pk_fma_f32 v[140:141], v[136:137], v[130:131], 1.0 op_sel_hi:[1,1,0]
	v_pk_fma_f32 v[150:151], v[148:149], v[144:145], 1.0 op_sel_hi:[1,1,0]
	v_pk_fma_f32 v[152:153], v[148:149], v[142:143], 1.0 op_sel_hi:[1,1,0]
	v_pk_fma_f32 v[184:185], v[182:183], v[178:179], 1.0 op_sel_hi:[1,1,0]
	v_pk_fma_f32 v[186:187], v[182:183], v[176:177], 1.0 op_sel_hi:[1,1,0]
	v_pk_fma_f32 v[240:241], v[238:239], v[234:235], 1.0 op_sel_hi:[1,1,0]
	v_pk_fma_f32 v[242:243], v[238:239], v[232:233], 1.0 op_sel_hi:[1,1,0]
	v_cvt_pk_bf16_f32 v154, v138, v139
	v_cvt_pk_bf16_f32 v155, v140, v141
	v_cvt_pk_bf16_f32 v156, v150, v151
	v_cvt_pk_bf16_f32 v157, v152, v153
	v_cvt_pk_bf16_f32 v158, v184, v185
	v_cvt_pk_bf16_f32 v159, v186, v187
	v_cvt_pk_bf16_f32 v160, v240, v241
	v_cvt_pk_bf16_f32 v161, v242, v243
	ds_read_b128 v[22:25], v172 offset:512
	ds_read_b128 v[6:9], v172 offset:576
	ds_read_b128 v[30:33], v172 offset:640
	ds_read_b128 v[14:17], v172 offset:704
	v_permlane16_swap_b32_e32 v154, v156
	v_permlane16_swap_b32_e32 v155, v157
	global_store_dwordx4 v228, v[154:157], s[64:65] offset:2048 nt
	v_permlane16_swap_b32_e32 v158, v160
	v_permlane16_swap_b32_e32 v159, v161
	global_store_dwordx4 v228, v[158:161], s[64:65] offset:2176 nt
	v_log_f32_e32 v166, v162
	v_log_f32_e32 v170, v174
	v_add_f32_e32 v168, v164, v165
	v_mul_f32_e32 v168, 0xbeb17218, v168
	v_add_f32_e32 v166, v166, v170
	v_fmac_f32_e32 v168, 0x3f317218, v166
	v_mov_b32_e32 v169, v168
	s_nop 1
	v_permlane16_swap_b32_e32 v168, v169
	v_add_f32_e32 v168, v168, v169
	v_mov_b32_e32 v169, v168
	s_nop 1
	v_permlane32_swap_b32_e32 v168, v169
	v_add_f32_e32 v168, v168, v169
	s_mov_b64 exec, s[0:1]
	global_store_dword v229, v168, s[66:67] offset:576
	s_mov_b64 exec, -1
	s_cmp_eq_u32 s40, 8
	s_cbranch_scc1 .Lg1_last_tile
	s_mov_b32 s2, s40
	s_add_i32 s40, s40, 1
	s_mov_b32 s41, s12
	s_lshl_b32 s12, s40, 5
	s_cmp_eq_u32 s2, 7
	s_cselect_b64 s[2:3], -1, 0
	s_and_b64 s[16:17], s[2:3], exec
	s_cselect_b32 s12, 0xe0, s12
	s_add_i32 s16, s12, s18
	s_lshr_b32 s12, s16, 4
	s_and_b32 s12, s12, 0xfffff8
	s_lshl_b32 s16, s16, 5
	s_mov_b32 s42, s35
	s_or_b32 s12, s12, s19
	s_and_b32 s35, s16, 0xf00
	s_lshl_b32 s16, s40, 10
	s_lshl_b32 s12, s12, 8
	s_and_b32 s43, s16, 0x400
	s_or_b64 s[2:3], vcc, s[2:3]
	s_lshl_b32 s44, s41, 7
	v_lshl_add_u64 v[202:203], s[12:13], 2, v[196:197]
	s_mov_b32 s45, 0x404000
	s_xor_b64 s[2:3], s[2:3], -1
	v_add_u32_e32 v194, s43, v208
	s_mov_b32 s46, 0
	s_bitcmp1_b32 s20, 12
	s_cbranch_scc0 .Lg1_noY
	s_barrier
